# lever 1 (counted waits): GDN chunk-local unit head waits vmcnt(12) instead of vmcnt(0): the previous unit's last 12 wide stores stay in flight; the prefetched rows are older and complete
# speedup vs baseline: 1.0090x; 1.0090x over previous
.LBB0_1464:
	s_andn2_b64 vcc, exec, s[0:1]
	s_cbranch_vccnz .LBB0_1576
	s_add_u32 s50, s46, 0x2d0f8000
	s_addc_u32 s51, s47, 0
	s_add_u32 s52, s46, 0x2b228000
	s_addc_u32 s53, s47, 0
	s_add_u32 s54, s46, 0x2b118000
	s_addc_u32 s55, s47, 0
	s_ashr_i32 s17, s16, 31
	s_mul_hi_i32 s8, s16, 0x600
	s_mul_i32 s9, s16, 0x600
	s_lshl_b64 s[56:57], s[16:17], 15
	s_lshl_b64 s[58:59], s[16:17], 14
	s_waitcnt vmcnt(0)
	s_branch .LBB0_1467

.LBB0_1467:
	v_mov_b32_e32 v61, v3
	v_mov_b32_e32 v0, v68
	s_waitcnt vmcnt(12)
	v_lshrrev_b32_e32 v9, 16, v36
	v_and_b32_e32 v21, 63, v0
	v_mul_u32_u24_e32 v1, 0x88, v21
	v_ashrrev_i32_e32 v60, 3, v0
	v_lshl_add_u32 v1, v1, 1, v61
	v_and_b32_e32 v4, -8, v60
	v_lshl_add_u32 v6, v4, 1, v1
	v_bitop3_b32 v27, v0, 63, v0 bitop3:0xc
	ds_write_b128 v6, v[40:43] offset:18432
	ds_write_b128 v6, v[36:39]
	v_mul_lo_u32 v6, v4, s33
	v_add_u32_e32 v5, 0x16800, v61
	v_add_u32_e32 v7, v61, v6
	v_lshlrev_b32_e32 v11, 1, v21
	v_lshlrev_b32_e32 v13, 1, v27
	v_add_u32_e32 v2, 0x12000, v61
	v_add_u32_e32 v8, v5, v6
	v_add_u32_e32 v12, v7, v11
	v_add_u32_e32 v14, v7, v13
	v_sub_u32_e32 v7, v7, v11
	v_lshrrev_b32_e32 v10, 16, v44
	ds_write_b16 v12, v36 offset:36864
	ds_write_b16 v12, v9 offset:37008
	ds_write_b16 v14, v36 offset:55296
	ds_write_b16 v7, v9 offset:55566
	v_add3_u32 v6, v2, v6, v11
	v_add_u32_e32 v9, v8, v13
	v_sub_u32_e32 v8, v8, v11
	ds_write_b16 v6, v44
	ds_write_b16 v6, v10 offset:144
	ds_write_b16 v9, v44
	ds_write_b16 v8, v10 offset:270
	v_lshrrev_b32_e32 v9, 16, v37
	v_lshrrev_b32_e32 v10, 16, v45
	v_add_u32_e32 v33, 0x200, v0
	ds_write_b16 v12, v37 offset:37152
	ds_write_b16 v12, v9 offset:37296
	ds_write_b16 v7, v37 offset:55710
	ds_write_b16 v7, v9 offset:55854
	ds_write_b16 v6, v45 offset:288
	ds_write_b16 v6, v10 offset:432
	ds_write_b16 v8, v45 offset:414
	ds_write_b16 v8, v10 offset:558
	v_lshrrev_b32_e32 v9, 16, v38
	v_lshrrev_b32_e32 v10, 16, v46
	v_ashrrev_i32_e32 v71, 3, v33
	ds_write_b16 v12, v38 offset:37440
	ds_write_b16 v12, v9 offset:37584
	ds_write_b16 v7, v38 offset:55998
	ds_write_b16 v7, v9 offset:56142
	ds_write_b16 v6, v46 offset:576
	ds_write_b16 v6, v10 offset:720
	ds_write_b16 v8, v46 offset:702
	ds_write_b16 v8, v10 offset:846
	v_lshrrev_b32_e32 v9, 16, v39
	v_lshrrev_b32_e32 v10, 16, v47
	ds_write_b16 v12, v39 offset:37728
	ds_write_b16 v12, v9 offset:37872
	ds_write_b16 v7, v39 offset:56286
	ds_write_b16 v7, v9 offset:56430
	ds_write_b16 v6, v47 offset:864
	ds_write_b16 v6, v10 offset:1008
	ds_write_b16 v8, v47 offset:990
	ds_write_b16 v8, v10 offset:1134
	v_and_b32_e32 v6, -8, v71
	v_lshl_add_u32 v1, v6, 1, v1
	ds_write_b128 v1, v[48:51] offset:18432
	ds_write_b128 v1, v[52:55]
	v_mul_lo_u32 v1, v6, s33
	v_ashrrev_i32_e32 v26, 6, v0
	v_add_u32_e32 v7, v61, v1
	v_add_u32_e32 v5, v5, v1
	v_lshrrev_b32_e32 v8, 16, v52
	v_add_u32_e32 v10, v7, v11
	v_add_u32_e32 v12, v7, v13
	v_sub_u32_e32 v7, v7, v11
	v_add3_u32 v1, v2, v1, v11
	v_add_u32_e32 v2, v5, v13
	v_readfirstlane_b32 s10, v26
	v_lshrrev_b32_e32 v9, 16, v56
	ds_write_b16 v10, v52 offset:36864
	ds_write_b16 v10, v8 offset:37008
	ds_write_b16 v12, v52 offset:55296
	ds_write_b16 v7, v8 offset:55566
	ds_write_b16 v1, v56
	ds_write_b16 v1, v9 offset:144
	ds_write_b16 v2, v56
	v_sub_u32_e32 v2, v5, v11
	v_lshrrev_b32_e32 v5, 16, v53
	v_lshrrev_b32_e32 v8, 16, v57
	s_cmp_lt_i32 s10, 2
	v_lshlrev_b32_e32 v28, 2, v21
	v_add_u32_e32 v22, 0x23400, v61
	ds_write_b16 v2, v9 offset:270
	ds_write_b16 v10, v53 offset:37152
	ds_write_b16 v10, v5 offset:37296
	ds_write_b16 v7, v53 offset:55710
	ds_write_b16 v7, v5 offset:55854
	ds_write_b16 v1, v57 offset:288
	ds_write_b16 v1, v8 offset:432
	ds_write_b16 v2, v57 offset:414
	ds_write_b16 v2, v8 offset:558
	v_lshrrev_b32_e32 v5, 16, v54
	v_lshrrev_b32_e32 v8, 16, v58
	v_add_u32_e32 v23, 0x23200, v61
	s_cselect_b64 s[2:3], -1, 0
	s_cmp_gt_i32 s10, 1
	v_cmp_eq_u32_e32 vcc, 0, v21
	v_lshl_or_b32 v24, s10, 8, v28
	ds_write_b16 v10, v54 offset:37440
	ds_write_b16 v10, v5 offset:37584
	ds_write_b16 v7, v54 offset:55998
	ds_write_b16 v7, v5 offset:56142
	ds_write_b16 v1, v58 offset:576
	ds_write_b16 v1, v8 offset:720
	ds_write_b16 v2, v58 offset:702
	ds_write_b16 v2, v8 offset:846
	v_lshrrev_b32_e32 v5, 16, v55
	v_lshrrev_b32_e32 v8, 16, v59
	ds_write_b16 v10, v55 offset:37728
	ds_write_b16 v10, v5 offset:37872
	ds_write_b16 v7, v55 offset:56286
	ds_write_b16 v7, v5 offset:56430
	ds_write_b16 v1, v59 offset:864
	ds_write_b16 v1, v8 offset:1008
	ds_write_b16 v2, v59 offset:990
	ds_write_b16 v2, v8 offset:1134
	s_cbranch_scc1 .LBB0_1469
	v_mov_b32_e32 v1, v69
	s_nop 1
	v_add_f32_dpp v1, v1, v1 row_shr:1 row_mask:0xf bank_mask:0xf
	s_nop 1
	v_add_f32_dpp v1, v1, v1 row_shr:2 row_mask:0xf bank_mask:0xf
	s_nop 1
	v_add_f32_dpp v1, v1, v1 row_shr:4 row_mask:0xf bank_mask:0xf
	s_nop 1
	v_add_f32_dpp v1, v1, v1 row_shr:8 row_mask:0xf bank_mask:0xf
	s_nop 1
	v_add_f32_dpp v1, v1, v1 row_bcast:15 row_mask:0xa bank_mask:0xf
	s_nop 1
	v_add_f32_dpp v1, v1, v1 row_bcast:31 row_mask:0xc bank_mask:0xf
	s_nop 1
	v_add_u32_e32 v2, v23, v24
	ds_write_b32 v2, v1
	v_add_u32_e32 v1, v22, v24
	ds_write_b32 v1, v70
